# in-proj tail: idle workgroups of the last partial round convert 16 (was 32) weight tiles; the attention-phase conversion jobs take the rest (on top of v27)
# baseline (speedup 1.0000x reference)
.LBB0_367:
	s_cmp_eq_u32 s28, 3
	s_cbranch_scc1 .LBB0_486
	s_waitcnt lgkmcnt(0)
	s_mov_b32 s0, s29
	s_cmpk_lg_i32 s0, 0x100
	s_mov_b32 s0, s29
	s_cbranch_scc1 .LBB0_486
	s_abs_i32 s0, s0
	v_cvt_f32_u32_e32 v2, s0
	s_sub_i32 s1, 0, s0
	v_rcp_iflag_f32_e32 v2, v2
	s_nop 0
	v_mul_f32_e32 v2, 0x4f7ffffe, v2
	v_cvt_u32_f32_e32 v2, v2
	s_nop 0
	v_readfirstlane_b32 s9, v2
	s_mul_i32 s1, s1, s9
	s_mul_hi_u32 s1, s9, s1
	s_add_i32 s9, s9, s1
	s_mul_hi_u32 s1, s9, 0x77a
	s_mul_i32 s1, s1, s0
	s_sub_i32 s1, 0x77a, s1
	s_sub_i32 s9, s1, s0
	s_cmp_ge_u32 s1, s0
	s_cselect_b32 s1, s9, s1
	s_sub_i32 s9, s1, s0
	s_cmp_ge_u32 s1, s0
	s_cselect_b32 s0, s9, s1
	v_readlane_b32 s1, v254, 0
	s_mov_b32 s1, s1
	s_cmp_lt_i32 s1, s0
	s_cbranch_scc1 .LBB0_486
	v_readlane_b32 s1, v254, 0
	s_mov_b32 s1, s1
	s_sub_i32 s0, s1, s0
	s_lshl_b32 s59, s0, 4
	v_mov_b32 v2, v0
	s_nop 0
	v_readfirstlane_b32 s0, v2
	s_ashr_i32 s0, s0, 6
	s_add_i32 s58, s59, s0
	s_add_i32 s0, s28, 1
	s_addk_i32 s59, 0x31e8
	s_addk_i32 s58, 0x31d8
	s_cmp_lt_i32 s58, s59
	s_cselect_b64 s[30:31], -1, 0
	s_cmp_ge_i32 s58, s59
	s_cbranch_scc1 .LBB0_395
	s_cmpk_gt_i32 s58, 0x72f
	s_mov_b64 s[48:49], -1
	s_cbranch_scc0 .LBB0_392
	s_cmpk_gt_u32 s58, 0x777
	s_mov_b64 s[46:47], -1
	s_cbranch_scc0 .LBB0_389
	s_cmpk_gt_u32 s58, 0x7b7
	s_mov_b64 s[14:15], -1
	s_cbranch_scc0 .LBB0_387
	s_cmpk_gt_u32 s58, 0x937
	s_cbranch_scc0 .LBB0_384
	s_cmpk_gt_u32 s58, 0xa37
	s_cbranch_scc0 .LBB0_381
	s_cmpk_gt_u32 s58, 0x2a37
	s_cbranch_scc0 .LBB0_378
	s_add_i32 s1, s58, 0xffffd5c8
	s_lshr_b32 s70, s1, 8
	s_load_dwordx2 s[14:15], s[76:77], 0xc8
	s_load_dwordx2 s[38:39], s[76:77], 0x118
	s_lshl_b64 s[34:35], s[70:71], 20
	s_lshl_b32 s9, s0, 24
	s_add_u32 s36, s34, s9
	s_addc_u32 s37, s35, 0
	s_lshl_b64 s[34:35], s[36:37], 2
	s_waitcnt lgkmcnt(0)
	s_add_u32 s9, s14, s34
	s_addc_u32 s14, s15, s35
	s_lshl_b32 s15, s1, 2
	s_and_b32 s70, s15, 0x3c0
	s_lshl_b32 s15, s70, 12
	s_add_u32 s9, s9, s15
	s_addc_u32 s14, s14, 0
	s_lshl_b32 s1, s1, 6
	s_and_b32 s1, s1, 0x3c0
	s_lshl_b32 s15, s1, 2
	s_add_u32 s34, s9, s15
	s_addc_u32 s35, s14, 0
	s_lshl_b64 s[14:15], s[36:37], 1
	s_add_u32 s9, s38, s14
	s_addc_u32 s14, s39, s15
	s_lshl_b32 s1, s1, 11
	s_add_u32 s42, s9, s1
	s_addc_u32 s43, s14, 0
	s_mov_b64 s[14:15], 0
	s_mov_b64 s[38:39], s[70:71]

.LBB0_827:
	s_andn2_b64 vcc, exec, s[46:47]
	s_cbranch_vccnz .LBB0_940
	s_mul_hi_i32 s0, s9, 0x2e8ba2e9
	s_lshr_b32 s1, s0, 31
	s_ashr_i32 s0, s0, 1
	s_add_i32 s0, s0, s1
	s_mul_i32 s1, s0, -11
	s_add_i32 s1, s1, s9
	s_cmp_lt_i32 s1, 9
	s_cbranch_scc1 .LBB0_940
	s_lshl_b32 s0, s0, 1
	s_add_i32 s0, s0, s1
	s_add_i32 s0, s0, -9
	s_cmpk_gt_i32 s0, 0x1d1
	s_cbranch_scc1 .LBB0_940
	v_readlane_b32 s14, v254, 3
	v_readlane_b32 s15, v254, 4
	s_load_dword s1, s[14:15], 0x0
	s_waitcnt lgkmcnt(0)
	s_mov_b32 s1, s1
	s_cmpk_eq_i32 s1, 0x100
	s_movk_i32 s1, 0x3a38
	s_cselect_b32 s1, 0x31d8, s1
	s_lshl_b32 s0, s0, 5
	s_cmp_le_i32 s1, s0
	s_cbranch_scc1 .LBB0_940
	s_add_i32 s9, s0, 32
	s_min_i32 s52, s9, s1
	v_mov_b32 v2, v0
	s_nop 0
	v_readfirstlane_b32 s1, v2
	s_ashr_i32 s59, s1, 6
	s_add_i32 s59, s59, s0
	s_cmp_lt_i32 s59, s52
	s_cselect_b64 s[86:87], -1, 0
	s_cmp_ge_i32 s59, s52
	s_cbranch_scc1 .LBB0_856
	s_cmpk_gt_i32 s59, 0x72f
	s_mov_b64 s[42:43], -1
	s_cbranch_scc0 .LBB0_853
	s_cmpk_gt_u32 s59, 0x777
	s_cbranch_scc0 .LBB0_850
	s_cmpk_gt_u32 s59, 0x7b7
	s_mov_b64 s[14:15], -1
	s_cbranch_scc0 .LBB0_848
	s_cmpk_gt_u32 s59, 0x937
	s_mov_b64 s[0:1], -1
	s_cbranch_scc0 .LBB0_845
	s_cmpk_gt_u32 s59, 0xa37
	s_cbranch_scc0 .LBB0_842
	s_cmpk_gt_u32 s59, 0x2a37
	s_cbranch_scc0 .LBB0_839
	s_add_i32 s9, s59, 0xffffd5c8
	s_lshr_b32 s70, s9, 8
	s_load_dwordx2 s[0:1], s[76:77], 0xc8
	s_load_dwordx2 s[34:35], s[76:77], 0x118
	s_lshl_b64 s[14:15], s[70:71], 20
	s_add_u32 s14, s14, s62
	s_addc_u32 s15, s15, s63
	s_lshl_b64 s[30:31], s[14:15], 2
	s_waitcnt lgkmcnt(0)
	s_add_u32 s0, s0, s30
	s_addc_u32 s1, s1, s31
	s_lshl_b32 s30, s9, 2
	s_and_b32 s70, s30, 0x3c0
	s_lshl_b32 s30, s70, 12
	s_add_u32 s0, s0, s30
	s_addc_u32 s1, s1, 0
	s_lshl_b32 s9, s9, 6
	s_and_b32 s9, s9, 0x3c0
	s_lshl_b32 s30, s9, 2
	s_add_u32 s30, s0, s30
	s_addc_u32 s31, s1, 0
	s_lshl_b64 s[0:1], s[14:15], 1
	s_add_u32 s0, s34, s0
	s_addc_u32 s1, s35, s1
	s_lshl_b32 s9, s9, 11
	s_add_u32 s34, s0, s9
	s_addc_u32 s35, s1, 0
	s_mov_b64 s[0:1], 0
	s_mov_b64 s[38:39], s[70:71]
